# speedup vs baseline: 1.1063x; 1.0161x over previous
_Z6k_gemmPKfS0_PK15HIP_vector_typeIjLj4EEPDF16_PKh:
	s_load_dwordx4 s[20:23], s[0:1], 0x0
	s_load_dwordx4 s[4:7], s[0:1], 0x10
	s_load_dwordx2 s[38:39], s[0:1], 0x20
	v_readfirstlane_b32 s8, v0
	v_and_b32_e32 v1, 63, v0
	s_nop 3
	s_lshr_b32 s8, s8, 6
	s_and_b32 s40, s2, 7
	s_lshr_b32 s41, s2, 3
	s_mul_i32 s18, s40, 0x187
	s_add_u32 s19, s18, 0x187
	s_min_u32 s19, s19, 0xc35
	s_sub_u32 s33, s19, s18
	s_sub_u32 s33, s33, 0x180
	s_lshl_b32 s33, s33, 2
	s_cmp_lt_u32 s41, s33
	s_cselect_b32 s44, 7, 6
	s_lshr_b32 s45, s41, 2
	s_add_u32 s45, s45, s18
	s_add_u32 s45, s45, 0x180
	s_lshl_b32 s45, s45, 4
	s_and_b32 s46, s41, 3
	s_lshl_b32 s46, s46, 2
	s_add_u32 s47, s45, s46
	s_mul_i32 s45, s47, 0x4b0
	s_lshl_b32 s46, s47, 8
	s_add_i32 s18, s18, s41
	s_cmp_eq_u32 s8, 0
	s_cselect_b32 s9, s44, 6
	s_add_i32 s11, s44, 4
	s_lshl_b32 s18, s18, 4
	s_lshl_b32 s19, s8, 2
	s_add_i32 s33, s18, s19
	s_mul_i32 s12, s33, 0x4b0
	s_lshl_b32 s32, s18, 8
	s_sub_u32 s32, s32, 0x100000
	s_mov_b32 s10, 0
	v_lshl_add_u32 v253, v1, 10, s33
	v_mov_b32_e32 v254, s47
	v_cmp_eq_u32_e32 vcc, 6, v1
	s_nop 1
	v_cndmask_b32_e32 v253, v253, v254, vcc
	v_mov_b32_e32 v247, 0
	v_cmp_gt_i32_e32 vcc, s9, v1
	s_mov_b32 s18, 0xc350
	v_cmp_gt_i32_e64 s[36:37], s18, v253
	s_and_b64 vcc, vcc, s[36:37]
	s_waitcnt lgkmcnt(0)
	s_and_saveexec_b64 s[36:37], vcc
	global_load_dword v247, v253, s[38:39]
	s_mov_b64 exec, s[36:37]
	s_mov_b32 s24, s22
	s_and_b32 s25, s23, 0xffff
	s_mov_b32 s26, 0x3938700
	s_mov_b32 s27, 0x20000
	s_and_b32 s21, s21, 0xffff
	s_mov_b32 s22, 0x3938700
	s_mov_b32 s23, 0x20000
	s_mov_b32 s28, s6
	s_and_b32 s29, s7, 0xffff
	s_mov_b32 s30, 0xc35000
	s_mov_b32 s31, 0x20000
	v_lshlrev_b32_e32 v238, 4, v1
	v_mul_u32_u24_e32 v253, 0x1746, v1
	v_lshrrev_b32_e32 v253, 16, v253
	v_min_u32_e32 v253, 3, v253
	v_mul_u32_u24_e32 v254, 11, v253
	v_sub_u32_e32 v254, v1, v254
	v_lshlrev_b32_e32 v240, 3, v253
	v_mul_u32_u24_e32 v249, 0x4b0, v253
	v_lshl_add_u32 v249, v254, 4, v249
	v_add_u32_e32 v249, 0x400, v249
	v_mov_b32_e32 v255, 0x80000000
	v_cmp_gt_u32_e64 s[34:35], 44, v1
	s_nop 1
	v_cndmask_b32_e64 v239, v255, v249, s[34:35]
	v_lshl_add_u32 v250, s8, 2, v253
	v_mul_u32_u24_e32 v250, 0x4e0, v250
	v_lshl_add_u32 v250, v254, 3, v250
	v_add_u32_e32 v242, 0x200, v250
	s_mul_i32 s18, s8, 0x1380
	v_lshl_add_u32 v241, v1, 3, s18
	v_and_b32_e32 v249, 15, v1
	v_lshrrev_b32_e32 v250, 4, v1
	v_mul_u32_u24_e32 v243, 0x4e0, v249
	v_lshl_add_u32 v243, v250, 4, v243
	v_mul_u32_u24_e32 v244, 0x440, v250
	v_lshl_add_u32 v244, v249, 1, v244
	s_lshl_b32 s18, s8, 6
	s_add_i32 s18, s18, 39936
	v_add_u32_e32 v244, s18, v244
	v_lshrrev_b32_e32 v249, 4, v0
	v_and_b32_e32 v250, 15, v0
	v_mul_u32_u24_e32 v245, 0x110, v249
	v_lshl_add_u32 v245, v250, 4, v245
	v_add_u32_e32 v245, 39936, v245
	v_lshlrev_b32_e32 v246, 8, v249
	v_lshl_add_u32 v246, v250, 4, v246
	s_lshl_b32 s18, s8, 12
	s_add_i32 s18, s18, 48640
	v_lshl_add_u32 v248, v1, 4, s18
	v_cmp_gt_u32_e32 vcc, 32, v0
	s_and_saveexec_b64 s[36:37], vcc
	v_mul_u32_u24_e32 v251, 0x4e00, v249
	v_mul_u32_u24_e32 v252, 0x4e0, v250
	v_add_u32_e32 v254, v251, v252
	v_mov_b32_e32 v250, 0
	v_mov_b32_e32 v251, 0
	v_mov_b32_e32 v252, 0
	v_mov_b32_e32 v253, 0
	ds_write_b128 v254, v[250:253] offset:1200
	s_mov_b64 exec, s[36:37]
	s_lshl_b32 s18, s8, 11
	v_lshl_add_u32 v253, v1, 4, s18
	v_add_u32_e32 v254, 0x22000, v253
	global_load_dwordx4 v[178:181], v254, s[4:5]
	global_load_dwordx4 v[182:185], v254, s[4:5] offset:1024
	v_add_u32_e32 v254, 0x2000, v254
	global_load_dwordx4 v[186:189], v254, s[4:5]
	global_load_dwordx4 v[190:193], v254, s[4:5] offset:1024
	v_mov_b32_e32 v236, v253
	s_waitcnt vmcnt(4)
	v_readlane_b32 s13, v247, s10
	s_add_u32 s14, s12, 0x4b0
	s_add_u32 s15, s12, 0x960
	s_add_u32 s16, s12, 0xe10
	s_nop 1
	s_and_b32 s18, s13, 0xff
	s_cmp_eq_u32 s18, 1
	s_cselect_b32 s42, s12, 0x80000000
	s_and_b32 s18, s13, 0xff00
	s_cmp_eq_u32 s18, 0x100
	s_cselect_b32 s14, s14, 0x80000000
	s_and_b32 s18, s13, 0xff0000
	s_cmp_eq_u32 s18, 0x10000
	s_cselect_b32 s15, s15, 0x80000000
	s_and_b32 s18, s13, 0xff000000
	s_cmp_eq_u32 s18, 0x1000000
	s_cselect_b32 s16, s16, 0x80000000
	v_lshrrev_b32_e64 v249, v240, s13
	v_and_b32_e32 v249, 0xff, v249
	v_cmp_eq_u32_e32 vcc, 1, v249
	s_nop 1
	v_cndmask_b32_e32 v254, v255, v239, vcc
	buffer_load_dwordx4 v[138:141], v238, s[20:23], s42 offen nt
	buffer_load_dwordx4 v[142:145], v238, s[24:27], s42 offen nt
	buffer_load_dwordx4 v[146:149], v238, s[20:23], s14 offen nt
	buffer_load_dwordx4 v[150:153], v238, s[24:27], s14 offen nt
	buffer_load_dwordx4 v[154:157], v238, s[20:23], s15 offen nt
	buffer_load_dwordx4 v[158:161], v238, s[24:27], s15 offen nt
	buffer_load_dwordx4 v[162:165], v238, s[20:23], s16 offen nt
	buffer_load_dwordx4 v[166:169], v238, s[24:27], s16 offen nt
	buffer_load_dwordx4 v[170:173], v254, s[20:23], s12 offen nt
	buffer_load_dwordx4 v[174:177], v254, s[24:27], s12 offen nt
	s_add_u32 s12, s12, 0x12c000
	s_add_u32 s32, s32, 0x40000
	s_mov_b32 s19, 0x80000000
	buffer_store_dwordx4 v[226:229], v246, s[28:31], s19 offen nt
	s_mov_b32 s10, 1
	global_load_dwordx4 v[2:5], v236, s[4:5]
	global_load_dwordx4 v[6:9], v236, s[4:5] offset:1024
	v_add_u32_e32 v236, 0x2000, v236
	global_load_dwordx4 v[10:13], v236, s[4:5]
	global_load_dwordx4 v[14:17], v236, s[4:5] offset:1024
	v_add_u32_e32 v236, 0x2000, v236
	global_load_dwordx4 v[18:21], v236, s[4:5]
	global_load_dwordx4 v[22:25], v236, s[4:5] offset:1024
	v_add_u32_e32 v236, 0x2000, v236
	global_load_dwordx4 v[26:29], v236, s[4:5]
	global_load_dwordx4 v[30:33], v236, s[4:5] offset:1024
	v_add_u32_e32 v236, 0x2000, v236
	global_load_dwordx4 v[34:37], v236, s[4:5]
	global_load_dwordx4 v[38:41], v236, s[4:5] offset:1024
	v_add_u32_e32 v236, 0x2000, v236
	global_load_dwordx4 v[42:45], v236, s[4:5]
	global_load_dwordx4 v[46:49], v236, s[4:5] offset:1024
	v_add_u32_e32 v236, 0x2000, v236
	global_load_dwordx4 v[50:53], v236, s[4:5]
	global_load_dwordx4 v[54:57], v236, s[4:5] offset:1024
	v_add_u32_e32 v236, 0x2000, v236
	global_load_dwordx4 v[58:61], v236, s[4:5]
	global_load_dwordx4 v[62:65], v236, s[4:5] offset:1024
	v_add_u32_e32 v236, 0x2000, v236
	global_load_dwordx4 v[66:69], v236, s[4:5]
	global_load_dwordx4 v[70:73], v236, s[4:5] offset:1024
	v_add_u32_e32 v236, 0x2000, v236
	global_load_dwordx4 v[74:77], v236, s[4:5]
	global_load_dwordx4 v[78:81], v236, s[4:5] offset:1024
	v_add_u32_e32 v236, 0x2000, v236
	global_load_dwordx4 v[82:85], v236, s[4:5]
	global_load_dwordx4 v[86:89], v236, s[4:5] offset:1024
	v_add_u32_e32 v236, 0x2000, v236
	global_load_dwordx4 v[90:93], v236, s[4:5]
	global_load_dwordx4 v[94:97], v236, s[4:5] offset:1024
	v_add_u32_e32 v236, 0x2000, v236
	global_load_dwordx4 v[98:101], v236, s[4:5]
	global_load_dwordx4 v[102:105], v236, s[4:5] offset:1024
	v_add_u32_e32 v236, 0x2000, v236
	global_load_dwordx4 v[106:109], v236, s[4:5]
	global_load_dwordx4 v[110:113], v236, s[4:5] offset:1024
	v_add_u32_e32 v236, 0x2000, v236
	global_load_dwordx4 v[114:117], v236, s[4:5]
	global_load_dwordx4 v[118:121], v236, s[4:5] offset:1024
	v_add_u32_e32 v236, 0x2000, v236
	global_load_dwordx4 v[122:125], v236, s[4:5]
	global_load_dwordx4 v[126:129], v236, s[4:5] offset:1024
	v_add_u32_e32 v236, 0x2000, v236
	global_load_dwordx4 v[130:133], v236, s[4:5]
	global_load_dwordx4 v[134:137], v236, s[4:5] offset:1024
	s_waitcnt vmcnt(45)
	ds_write_b128 v248, v[178:181]
	ds_write_b128 v248, v[182:185] offset:1024
	ds_write_b128 v248, v[186:189] offset:2048
	ds_write_b128 v248, v[190:193] offset:3072
	s_waitcnt lgkmcnt(0)
	s_barrier
	s_branch .Lg_half1
.Lg_top:
	s_cmp_ge_u32 s10, s9
	s_cbranch_scc1 .Lg_noprep0
	s_cmp_eq_u32 s10, 6
	s_cselect_b32 s12, s45, s12
	v_readlane_b32 s13, v247, s10
	s_add_u32 s14, s12, 0x4b0
	s_add_u32 s15, s12, 0x960
	s_add_u32 s16, s12, 0xe10
	s_nop 1
	s_and_b32 s18, s13, 0xff
	s_cmp_eq_u32 s18, 1
	s_cselect_b32 s42, s12, 0x80000000
	s_and_b32 s18, s13, 0xff00
	s_cmp_eq_u32 s18, 0x100
	s_cselect_b32 s14, s14, 0x80000000
	s_and_b32 s18, s13, 0xff0000
	s_cmp_eq_u32 s18, 0x10000
	s_cselect_b32 s15, s15, 0x80000000
	s_and_b32 s18, s13, 0xff000000
	s_cmp_eq_u32 s18, 0x1000000
	s_cselect_b32 s16, s16, 0x80000000
	v_lshrrev_b32_e64 v249, v240, s13
	v_and_b32_e32 v249, 0xff, v249
	v_cmp_eq_u32_e32 vcc, 1, v249
	s_nop 1
	v_cndmask_b32_e32 v254, v255, v239, vcc

.Lg_s1done0:
	s_add_u32 s12, s12, 0x12c000
	s_sub_u32 s18, s10, 3
	s_cmp_lt_u32 s18, s44
	s_cbranch_scc0 .Lg_s3skip0
	ds_read_b128 v[226:229], v243 offset:21056
	ds_read_b128 v[230:233], v248
	ds_read_b128 v[234:237], v248 offset:1024
	s_waitcnt lgkmcnt(0)
	v_mfma_f32_16x16x32_f16 v[218:221], v[226:229], v[230:233], 0
	v_mfma_f32_16x16x32_f16 v[222:225], v[226:229], v[234:237], 0
	ds_read_b128 v[226:229], v243 offset:21120
	ds_read_b128 v[230:233], v248 offset:2048
	ds_read_b128 v[234:237], v248 offset:3072
	s_waitcnt lgkmcnt(0)
	v_mfma_f32_16x16x32_f16 v[218:221], v[226:229], v[230:233], v[218:221]
	v_mfma_f32_16x16x32_f16 v[222:225], v[226:229], v[234:237], v[222:225]
	ds_read_b128 v[226:229], v243 offset:19968
	ds_read_b128 v[230:233], v243 offset:20032
	ds_read_b128 v[234:237], v243 offset:20096
	s_waitcnt lgkmcnt(2)
	v_mfma_f32_16x16x32_f16 v[218:221], v[226:229], v[2:5], v[218:221]
	v_mfma_f32_16x16x32_f16 v[222:225], v[226:229], v[6:9], v[222:225]
	ds_read_b128 v[226:229], v243 offset:20160
	s_waitcnt lgkmcnt(2)
	v_mfma_f32_16x16x32_f16 v[218:221], v[230:233], v[10:13], v[218:221]
	v_mfma_f32_16x16x32_f16 v[222:225], v[230:233], v[14:17], v[222:225]
	ds_read_b128 v[230:233], v243 offset:20224
	s_waitcnt lgkmcnt(2)
	v_mfma_f32_16x16x32_f16 v[218:221], v[234:237], v[18:21], v[218:221]
	v_mfma_f32_16x16x32_f16 v[222:225], v[234:237], v[22:25], v[222:225]
	ds_read_b128 v[234:237], v243 offset:20288
	s_waitcnt lgkmcnt(2)
	v_mfma_f32_16x16x32_f16 v[218:221], v[226:229], v[26:29], v[218:221]
	v_mfma_f32_16x16x32_f16 v[222:225], v[226:229], v[30:33], v[222:225]
	ds_read_b128 v[226:229], v243 offset:20352
	s_waitcnt lgkmcnt(2)
	v_mfma_f32_16x16x32_f16 v[218:221], v[230:233], v[34:37], v[218:221]
	v_mfma_f32_16x16x32_f16 v[222:225], v[230:233], v[38:41], v[222:225]
	ds_read_b128 v[230:233], v243 offset:20416
	s_waitcnt lgkmcnt(2)
	v_mfma_f32_16x16x32_f16 v[218:221], v[234:237], v[42:45], v[218:221]
	v_mfma_f32_16x16x32_f16 v[222:225], v[234:237], v[46:49], v[222:225]
	ds_read_b128 v[234:237], v243 offset:20480
	s_waitcnt lgkmcnt(2)
	v_mfma_f32_16x16x32_f16 v[218:221], v[226:229], v[50:53], v[218:221]
	v_mfma_f32_16x16x32_f16 v[222:225], v[226:229], v[54:57], v[222:225]
	ds_read_b128 v[226:229], v243 offset:20544
	s_waitcnt lgkmcnt(2)
	v_mfma_f32_16x16x32_f16 v[218:221], v[230:233], v[58:61], v[218:221]
	v_mfma_f32_16x16x32_f16 v[222:225], v[230:233], v[62:65], v[222:225]
	ds_read_b128 v[230:233], v243 offset:20608
	s_waitcnt lgkmcnt(2)
	v_mfma_f32_16x16x32_f16 v[218:221], v[234:237], v[66:69], v[218:221]
	v_mfma_f32_16x16x32_f16 v[222:225], v[234:237], v[70:73], v[222:225]
	ds_read_b128 v[234:237], v243 offset:20672
	s_waitcnt lgkmcnt(2)
	v_mfma_f32_16x16x32_f16 v[218:221], v[226:229], v[74:77], v[218:221]
	v_mfma_f32_16x16x32_f16 v[222:225], v[226:229], v[78:81], v[222:225]
	ds_read_b128 v[226:229], v243 offset:20736
	s_waitcnt lgkmcnt(2)
	v_mfma_f32_16x16x32_f16 v[218:221], v[230:233], v[82:85], v[218:221]
	v_mfma_f32_16x16x32_f16 v[222:225], v[230:233], v[86:89], v[222:225]
	ds_read_b128 v[230:233], v243 offset:20800
	s_waitcnt lgkmcnt(2)
	v_mfma_f32_16x16x32_f16 v[218:221], v[234:237], v[90:93], v[218:221]
	v_mfma_f32_16x16x32_f16 v[222:225], v[234:237], v[94:97], v[222:225]
	ds_read_b128 v[234:237], v243 offset:20864
	s_waitcnt lgkmcnt(2)
	v_mfma_f32_16x16x32_f16 v[218:221], v[226:229], v[98:101], v[218:221]
	v_mfma_f32_16x16x32_f16 v[222:225], v[226:229], v[102:105], v[222:225]
	ds_read_b128 v[226:229], v243 offset:20928
	s_waitcnt lgkmcnt(2)
	v_mfma_f32_16x16x32_f16 v[218:221], v[230:233], v[106:109], v[218:221]
	v_mfma_f32_16x16x32_f16 v[222:225], v[230:233], v[110:113], v[222:225]
	ds_read_b128 v[230:233], v243 offset:20992
	s_waitcnt lgkmcnt(2)
	v_mfma_f32_16x16x32_f16 v[218:221], v[234:237], v[114:117], v[218:221]
	v_mfma_f32_16x16x32_f16 v[222:225], v[234:237], v[118:121], v[222:225]
	s_waitcnt lgkmcnt(1)
	v_mfma_f32_16x16x32_f16 v[218:221], v[226:229], v[122:125], v[218:221]
	v_mfma_f32_16x16x32_f16 v[222:225], v[226:229], v[126:129], v[222:225]
	s_waitcnt lgkmcnt(0)
	v_mfma_f32_16x16x32_f16 v[218:221], v[230:233], v[130:133], v[218:221]
	v_mfma_f32_16x16x32_f16 v[222:225], v[230:233], v[134:137], v[222:225]
	s_nop 7
	s_nop 3
	v_cvt_f16_f32_e32 v249, v218
	v_cvt_f16_f32_e32 v250, v219
	v_cvt_f16_f32_e32 v251, v220
	v_cvt_f16_f32_e32 v252, v221
	ds_write_b16 v244, v249 offset:4352
	ds_write_b16 v244, v250 offset:4624
	ds_write_b16 v244, v251 offset:4896
	ds_write_b16 v244, v252 offset:5168
	v_cvt_f16_f32_e32 v249, v222
	v_cvt_f16_f32_e32 v250, v223
	v_cvt_f16_f32_e32 v251, v224
	v_cvt_f16_f32_e32 v252, v225
	ds_write_b16 v244, v249 offset:4384
	ds_write_b16 v244, v250 offset:4656
	ds_write_b16 v244, v251 offset:4928
	ds_write_b16 v244, v252 offset:5200
.Lg_s3skip0:
	s_cmp_eq_u32 s10, 10
	s_cselect_b32 s32, s46, s32
	s_sub_u32 s18, s10, 4
	s_cmp_lt_u32 s18, s9
	s_cselect_b32 s19, s32, 0x80000000
	ds_read_b128 v[226:229], v245 offset:0
	s_add_u32 s32, s32, 0x40000
	s_waitcnt lgkmcnt(0)
	buffer_store_dwordx4 v[226:229], v246, s[28:31], s19 offen nt
	s_barrier
	s_add_u32 s10, s10, 1
	s_cmp_ge_u32 s10, s11
	s_cbranch_scc1 .Lg_end

.Lg_s1done1:
	s_add_u32 s12, s12, 0x12c000
	s_sub_u32 s18, s10, 3
	s_cmp_lt_u32 s18, s44
	s_cbranch_scc0 .Lg_s3skip1
	ds_read_b128 v[226:229], v243 offset:1088
	ds_read_b128 v[230:233], v248
	ds_read_b128 v[234:237], v248 offset:1024
	s_waitcnt lgkmcnt(0)
	v_mfma_f32_16x16x32_f16 v[218:221], v[226:229], v[230:233], 0
	v_mfma_f32_16x16x32_f16 v[222:225], v[226:229], v[234:237], 0
	ds_read_b128 v[226:229], v243 offset:1152
	ds_read_b128 v[230:233], v248 offset:2048
	ds_read_b128 v[234:237], v248 offset:3072
	s_waitcnt lgkmcnt(0)
	v_mfma_f32_16x16x32_f16 v[218:221], v[226:229], v[230:233], v[218:221]
	v_mfma_f32_16x16x32_f16 v[222:225], v[226:229], v[234:237], v[222:225]
	ds_read_b128 v[226:229], v243 offset:0
	ds_read_b128 v[230:233], v243 offset:64
	ds_read_b128 v[234:237], v243 offset:128
	s_waitcnt lgkmcnt(2)
	v_mfma_f32_16x16x32_f16 v[218:221], v[226:229], v[2:5], v[218:221]
	v_mfma_f32_16x16x32_f16 v[222:225], v[226:229], v[6:9], v[222:225]
	ds_read_b128 v[226:229], v243 offset:192
	s_waitcnt lgkmcnt(2)
	v_mfma_f32_16x16x32_f16 v[218:221], v[230:233], v[10:13], v[218:221]
	v_mfma_f32_16x16x32_f16 v[222:225], v[230:233], v[14:17], v[222:225]
	ds_read_b128 v[230:233], v243 offset:256
	s_waitcnt lgkmcnt(2)
	v_mfma_f32_16x16x32_f16 v[218:221], v[234:237], v[18:21], v[218:221]
	v_mfma_f32_16x16x32_f16 v[222:225], v[234:237], v[22:25], v[222:225]
	ds_read_b128 v[234:237], v243 offset:320
	s_waitcnt lgkmcnt(2)
	v_mfma_f32_16x16x32_f16 v[218:221], v[226:229], v[26:29], v[218:221]
	v_mfma_f32_16x16x32_f16 v[222:225], v[226:229], v[30:33], v[222:225]
	ds_read_b128 v[226:229], v243 offset:384
	s_waitcnt lgkmcnt(2)
	v_mfma_f32_16x16x32_f16 v[218:221], v[230:233], v[34:37], v[218:221]
	v_mfma_f32_16x16x32_f16 v[222:225], v[230:233], v[38:41], v[222:225]
	ds_read_b128 v[230:233], v243 offset:448
	s_waitcnt lgkmcnt(2)
	v_mfma_f32_16x16x32_f16 v[218:221], v[234:237], v[42:45], v[218:221]
	v_mfma_f32_16x16x32_f16 v[222:225], v[234:237], v[46:49], v[222:225]
	ds_read_b128 v[234:237], v243 offset:512
	s_waitcnt lgkmcnt(2)
	v_mfma_f32_16x16x32_f16 v[218:221], v[226:229], v[50:53], v[218:221]
	v_mfma_f32_16x16x32_f16 v[222:225], v[226:229], v[54:57], v[222:225]
	ds_read_b128 v[226:229], v243 offset:576
	s_waitcnt lgkmcnt(2)
	v_mfma_f32_16x16x32_f16 v[218:221], v[230:233], v[58:61], v[218:221]
	v_mfma_f32_16x16x32_f16 v[222:225], v[230:233], v[62:65], v[222:225]
	ds_read_b128 v[230:233], v243 offset:640
	s_waitcnt lgkmcnt(2)
	v_mfma_f32_16x16x32_f16 v[218:221], v[234:237], v[66:69], v[218:221]
	v_mfma_f32_16x16x32_f16 v[222:225], v[234:237], v[70:73], v[222:225]
	ds_read_b128 v[234:237], v243 offset:704
	s_waitcnt lgkmcnt(2)
	v_mfma_f32_16x16x32_f16 v[218:221], v[226:229], v[74:77], v[218:221]
	v_mfma_f32_16x16x32_f16 v[222:225], v[226:229], v[78:81], v[222:225]
	ds_read_b128 v[226:229], v243 offset:768
	s_waitcnt lgkmcnt(2)
	v_mfma_f32_16x16x32_f16 v[218:221], v[230:233], v[82:85], v[218:221]
	v_mfma_f32_16x16x32_f16 v[222:225], v[230:233], v[86:89], v[222:225]
	ds_read_b128 v[230:233], v243 offset:832
	s_waitcnt lgkmcnt(2)
	v_mfma_f32_16x16x32_f16 v[218:221], v[234:237], v[90:93], v[218:221]
	v_mfma_f32_16x16x32_f16 v[222:225], v[234:237], v[94:97], v[222:225]
	ds_read_b128 v[234:237], v243 offset:896
	s_waitcnt lgkmcnt(2)
	v_mfma_f32_16x16x32_f16 v[218:221], v[226:229], v[98:101], v[218:221]
	v_mfma_f32_16x16x32_f16 v[222:225], v[226:229], v[102:105], v[222:225]
	ds_read_b128 v[226:229], v243 offset:960
	s_waitcnt lgkmcnt(2)
	v_mfma_f32_16x16x32_f16 v[218:221], v[230:233], v[106:109], v[218:221]
	v_mfma_f32_16x16x32_f16 v[222:225], v[230:233], v[110:113], v[222:225]
	ds_read_b128 v[230:233], v243 offset:1024
	s_waitcnt lgkmcnt(2)
	v_mfma_f32_16x16x32_f16 v[218:221], v[234:237], v[114:117], v[218:221]
	v_mfma_f32_16x16x32_f16 v[222:225], v[234:237], v[118:121], v[222:225]
	s_waitcnt lgkmcnt(1)
	v_mfma_f32_16x16x32_f16 v[218:221], v[226:229], v[122:125], v[218:221]
	v_mfma_f32_16x16x32_f16 v[222:225], v[226:229], v[126:129], v[222:225]
	s_waitcnt lgkmcnt(0)
	v_mfma_f32_16x16x32_f16 v[218:221], v[230:233], v[130:133], v[218:221]
	v_mfma_f32_16x16x32_f16 v[222:225], v[230:233], v[134:137], v[222:225]
	s_nop 7
	s_nop 3
	v_cvt_f16_f32_e32 v249, v218
	v_cvt_f16_f32_e32 v250, v219
	v_cvt_f16_f32_e32 v251, v220
	v_cvt_f16_f32_e32 v252, v221
	ds_write_b16 v244, v249 offset:0
	ds_write_b16 v244, v250 offset:272
	ds_write_b16 v244, v251 offset:544
	ds_write_b16 v244, v252 offset:816
	v_cvt_f16_f32_e32 v249, v222
	v_cvt_f16_f32_e32 v250, v223
	v_cvt_f16_f32_e32 v251, v224
	v_cvt_f16_f32_e32 v252, v225
	ds_write_b16 v244, v249 offset:32
	ds_write_b16 v244, v250 offset:304
	ds_write_b16 v244, v251 offset:576
	ds_write_b16 v244, v252 offset:848
.Lg_s3skip1:
	s_cmp_eq_u32 s10, 10
	s_cselect_b32 s32, s46, s32
	s_sub_u32 s18, s10, 4
	s_cmp_lt_u32 s18, s9
	s_cselect_b32 s19, s32, 0x80000000
	ds_read_b128 v[226:229], v245 offset:4352
	s_add_u32 s32, s32, 0x40000
	s_waitcnt lgkmcnt(0)
	buffer_store_dwordx4 v[226:229], v246, s[28:31], s19 offen nt
	s_barrier
	s_add_u32 s10, s10, 1
	s_cmp_lt_u32 s10, s11
	s_cbranch_scc1 .Lg_top

	.amdhsa_kernel _Z6k_gemmPKfS0_PK15HIP_vector_typeIjLj4EEPDF16_PKh
		.amdhsa_group_segment_fixed_size 16384
		.amdhsa_private_segment_fixed_size 0
		.amdhsa_kernarg_size 40
		.amdhsa_user_sgpr_count 2
		.amdhsa_user_sgpr_dispatch_ptr 0
		.amdhsa_user_sgpr_queue_ptr 0
		.amdhsa_user_sgpr_kernarg_segment_ptr 1
		.amdhsa_user_sgpr_dispatch_id 0
		.amdhsa_user_sgpr_kernarg_preload_length 0
		.amdhsa_user_sgpr_kernarg_preload_offset 0
		.amdhsa_user_sgpr_private_segment_size 0
		.amdhsa_uses_dynamic_stack 0
		.amdhsa_enable_private_segment 0
		.amdhsa_system_sgpr_workgroup_id_x 1
		.amdhsa_system_sgpr_workgroup_id_y 0
		.amdhsa_system_sgpr_workgroup_id_z 0
		.amdhsa_system_sgpr_workgroup_info 0
		.amdhsa_system_vgpr_workitem_id 0
		.amdhsa_next_free_vgpr 256
		.amdhsa_next_free_sgpr 48
		.amdhsa_accum_offset 256
		.amdhsa_reserve_vcc 1
		.amdhsa_float_round_mode_32 0
		.amdhsa_float_round_mode_16_64 0
		.amdhsa_float_denorm_mode_32 3
		.amdhsa_float_denorm_mode_16_64 3
		.amdhsa_dx10_clamp 1
		.amdhsa_ieee_mode 1
		.amdhsa_fp16_overflow 0
		.amdhsa_tg_split 0
		.amdhsa_exception_fp_ieee_invalid_op 0
		.amdhsa_exception_fp_denorm_src 0
		.amdhsa_exception_fp_ieee_div_zero 0
		.amdhsa_exception_fp_ieee_overflow 0
		.amdhsa_exception_fp_ieee_underflow 0
		.amdhsa_exception_fp_ieee_inexact 0
		.amdhsa_exception_int_div_zero 0
	.end_amdhsa_kernel

amdhsa.kernels:
  - .agpr_count:     0
    .args:
      - .actual_access:  read_only
        .address_space:  global
        .offset:         0
        .size:           8
        .value_kind:     global_buffer
      - .actual_access:  read_only
        .address_space:  global
        .offset:         8
        .size:           8
        .value_kind:     global_buffer
      - .actual_access:  write_only
        .address_space:  global
        .offset:         16
        .size:           8
        .value_kind:     global_buffer
      - .actual_access:  write_only
        .address_space:  global
        .offset:         24
        .size:           8
        .value_kind:     global_buffer
      - .actual_access:  write_only
        .address_space:  global
        .offset:         32
        .size:           8
        .value_kind:     global_buffer
      - .actual_access:  write_only
        .address_space:  global
        .offset:         40
        .size:           8
        .value_kind:     global_buffer
    .group_segment_fixed_size: 32
    .kernarg_segment_align: 8
    .kernarg_segment_size: 48
    .language:       OpenCL C
    .language_version:
      - 2
      - 0
    .max_flat_workgroup_size: 512
    .name:           _Z6k_prepPKiPKfPiS3_P15HIP_vector_typeIjLj4EEPh
    .private_segment_fixed_size: 0
    .sgpr_count:     16
    .sgpr_spill_count: 0
    .symbol:         _Z6k_prepPKiPKfPiS3_P15HIP_vector_typeIjLj4EEPh.kd
    .uniform_work_group_size: 1
    .uses_dynamic_stack: false
    .vgpr_count:     36
    .vgpr_spill_count: 0
    .wavefront_size: 64
  - .agpr_count:     0
    .args:
      - .actual_access:  read_only
        .address_space:  global
        .offset:         0
        .size:           8
        .value_kind:     global_buffer
      - .actual_access:  read_only
        .address_space:  global
        .offset:         8
        .size:           8
        .value_kind:     global_buffer
      - .actual_access:  read_only
        .address_space:  global
        .offset:         16
        .size:           8
        .value_kind:     global_buffer
      - .actual_access:  write_only
        .address_space:  global
        .offset:         24
        .size:           8
        .value_kind:     global_buffer
      - .actual_access:  read_only
        .address_space:  global
        .offset:         32
        .size:           8
        .value_kind:     global_buffer
    .group_segment_fixed_size: 16384
    .kernarg_segment_align: 8
    .kernarg_segment_size: 40
    .language:       OpenCL C
    .language_version:
      - 2
      - 0
    .max_flat_workgroup_size: 256
    .name:           _Z6k_gemmPKfS0_PK15HIP_vector_typeIjLj4EEPDF16_PKh
    .private_segment_fixed_size: 0
    .sgpr_count:     54
    .sgpr_spill_count: 0
    .symbol:         _Z6k_gemmPKfS0_PK15HIP_vector_typeIjLj4EEPDF16_PKh.kd
    .uniform_work_group_size: 1
    .uses_dynamic_stack: false
    .vgpr_count:     256
    .vgpr_spill_count: 0
    .wavefront_size: 64
  - .agpr_count:     0
    .args:
      - .actual_access:  read_only
        .address_space:  global
        .offset:         0
        .size:           8
        .value_kind:     global_buffer
      - .actual_access:  read_only
        .address_space:  global
        .offset:         8
        .size:           8
        .value_kind:     global_buffer
      - .actual_access:  read_only
        .address_space:  global
        .offset:         16
        .size:           8
        .value_kind:     global_buffer
      - .actual_access:  read_only
        .address_space:  global
        .offset:         24
        .size:           8
        .value_kind:     global_buffer
      - .actual_access:  read_only
        .address_space:  global
        .offset:         32
        .size:           8
        .value_kind:     global_buffer
      - .actual_access:  read_only
        .address_space:  global
        .offset:         40
        .size:           8
        .value_kind:     global_buffer
      - .actual_access:  write_only
        .address_space:  global
        .offset:         48
        .size:           8
        .value_kind:     global_buffer
    .group_segment_fixed_size: 4096
    .kernarg_segment_align: 8
    .kernarg_segment_size: 56
    .language:       OpenCL C
    .language_version:
      - 2
      - 0
    .max_flat_workgroup_size: 1024
    .name:           _Z6k_poolPKDF16_PKiS2_PKfS4_S4_Pf
    .private_segment_fixed_size: 0
    .sgpr_count:     30
    .sgpr_spill_count: 0
    .symbol:         _Z6k_poolPKDF16_PKiS2_PKfS4_S4_Pf.kd
    .uniform_work_group_size: 1
    .uses_dynamic_stack: false
    .vgpr_count:     64
    .vgpr_spill_count: 0
    .wavefront_size: 64
